# inproj q/k epilogue: cross-lane sums of squares via v_permlane16/32_swap instead of two dependent ds_bpermute round trips per 16-row block
# speedup vs baseline: 1.0041x; 1.0041x over previous
;     __device__ __forceinline__ void operator()(const pg8::i32x4 (&acc)[2][2][4][2], const Unit& u, int wr, int wc, int fr, int fq) const {
;     ...
;         if (pn < 4) {
;             const bool isq = pn < 2; bf16_t* base = (bf16_t*)(U + (isq ? U_Q : U_K)); const float* nw = qkw + (isq ? 0 : 64); const float osc = isq ? 0.125f * LOG2E : 1.f;
;             const int hg = 4 * (pn & 1) + wc;
;             f32x4 w[2][2];
; #pragma unroll
;             for (int bj = 0; bj < 2; ++bj)
; #pragma unroll
;                 for (int n = 0; n < 2; ++n) w[bj][n] = *(const f32x4*)(nw + 32 * bj + 16 * n + 4 * fq);
; #pragma unroll
;             for (int ai = 0; ai < 2; ++ai)
; #pragma unroll
;                 for (int m = 0; m < 4; ++m) {
;                     const int row = u.pm * 256 + ai * 128 + wr * 64 + m * 16 + fr;
;                     float ss = 0.f; const float sa = sah[row]; f32x4 xf[2][2];
; #pragma unroll
;                     for (int bj = 0; bj < 2; ++bj)
; #pragma unroll
;                         for (int n = 0; n < 2; ++n) { f32x4 x;
; #pragma unroll
;                             for (int i = 0; i < 4; ++i) x[i] = (float)acc[ai][bj][m][n][i] * (sa * swv[bj][n][i]);
;                             xf[bj][n] = x; ss += x[0] * x[0] + x[1] * x[1] + x[2] * x[2] + x[3] * x[3]; }
;                     { const int ln = fq * 16 + fr; ss += shx(ss, 16, ln); ss += shx(ss, 32, ln); }
;                     const float rstd = rsqrtf(ss * (1.f / 64.f) + EPS);
;                     const bool lat = row < NL; const int tok = row & 2047;
; #pragma unroll
;                     for (int bj = 0; bj < 2; ++bj) {
;                         f32x4 x1 = xf[bj][0] * rstd * w[bj][0], x2 = xf[bj][1] * rstd * w[bj][1];
;                         if (lat) { const int pos = bj ? (tok & 63) : (tok >> 6); const f32x4 c = *(const f32x4*)(ropec + pos * 16 + 4 * fq), s = *(const f32x4*)(ropes + pos * 16 + 4 * fq);
;                             const f32x4 o1 = x1 * c - x2 * s, o2 = x1 * s + x2 * c; x1 = o1; x2 = o2; }
;                         x1 = x1 * osc; x2 = x2 * osc;
;                         bf16_t* p = base + (size_t)row * 512 + 64 * hg + 32 * bj + 4 * fq;
;                         *(u32x2*)p = (u32x2){pk2(x1[0], x1[1]), pk2(x1[2], x1[3])};
;                         *(u32x2*)(p + 16) = (u32x2){pk2(x2[0], x2[1]), pk2(x2[2], x2[3])};
;                     }
.LBB0_288:
	s_cmp_lt_i32 s56, 2
	s_cselect_b64 vcc, -1, 0
	s_and_b64 s[2:3], vcc, exec
	s_cselect_b32 s30, 0, 0x100
	s_lshl_b32 s4, s40, 8
	s_add_i32 s4, s4, s11
	v_or_b32_e32 v196, s4, v198
	v_lshlrev_b32_e32 v224, 2, v196
	global_load_dword v216, v224, s[44:45]
	global_load_dword v217, v224, s[44:45] offset:64
	global_load_dword v218, v224, s[44:45] offset:128
	global_load_dword v219, v224, s[44:45] offset:192
	global_load_dword v220, v224, s[44:45] offset:512
	global_load_dword v221, v224, s[44:45] offset:576
	global_load_dword v222, v224, s[44:45] offset:640
	global_load_dword v223, v224, s[44:45] offset:704
	v_mbcnt_lo_u32_b32 v225, -1, 0
	v_mbcnt_hi_u32_b32 v225, -1, v225
	v_and_b32_e32 v225, 48, v225
	v_add_u32_e32 v225, 0x20000, v225
	v_lshl_add_u32 v226, v198, 6, v225
	v_ashrrev_i32_e32 v197, 31, v196
	v_lshl_add_u64 v[20:21], v[152:153], 0, s[30:31]
	v_lshl_add_u64 v[36:37], v[196:197], 2, s[44:45]
	global_load_dwordx4 v[32:35], v[20:21], off
	global_load_dwordx4 v[28:31], v[20:21], off offset:64
	global_load_dwordx4 v[24:27], v[20:21], off offset:128
	s_nop 0
	global_load_dwordx4 v[20:23], v[20:21], off offset:192
	s_mov_b32 s2, 0x8000
	s_waitcnt vmcnt(0)
	v_mov_b32_e32 v0, v216
	v_pk_mul_f32 v[36:37], v[16:17], v[0:1] op_sel_hi:[1,0]
	v_pk_mul_f32 v[118:119], v[12:13], v[0:1] op_sel_hi:[1,0]
	v_pk_mul_f32 v[36:37], v[36:37], v[194:195]
	v_pk_mul_f32 v[118:119], v[118:119], v[190:191]
	v_pk_mul_f32 v[128:129], v[14:15], v[0:1] op_sel_hi:[1,0]
	v_pk_mul_f32 v[38:39], v[18:19], v[0:1] op_sel_hi:[1,0]
	v_pk_mul_f32 v[128:129], v[128:129], v[188:189]
	v_mov_b32_e32 v188, v37
	v_mov_b32_e32 v189, v119
	v_pk_mul_f32 v[38:39], v[38:39], v[192:193]
	v_mov_b32_e32 v178, v36
	v_mov_b32_e32 v179, v118
	v_pk_mul_f32 v[188:189], v[188:189], v[188:189]
	s_nop 0
	v_pk_fma_f32 v[178:179], v[178:179], v[178:179], v[188:189]
	v_mov_b32_e32 v188, v38
	v_mov_b32_e32 v189, v128
	v_pk_fma_f32 v[178:179], v[188:189], v[188:189], v[178:179]
	v_mov_b32_e32 v188, v39
	v_mov_b32_e32 v189, v129
	v_pk_fma_f32 v[178:179], v[188:189], v[188:189], v[178:179]
	v_pk_mul_f32 v[188:189], v[8:9], v[0:1] op_sel_hi:[1,0]
	s_nop 0
	v_pk_mul_f32 v[186:187], v[188:189], v[186:187]
	v_pk_mul_f32 v[188:189], v[10:11], v[0:1] op_sel_hi:[1,0]
	v_mov_b32_e32 v191, v187
	v_pk_mul_f32 v[184:185], v[188:189], v[184:185]
	v_pk_mul_f32 v[188:189], v[4:5], v[0:1] op_sel_hi:[1,0]
	s_nop 0
	v_pk_mul_f32 v[182:183], v[188:189], v[182:183]
	v_pk_mul_f32 v[188:189], v[6:7], v[0:1] op_sel_hi:[1,0]
	v_mov_b32_e32 v190, v183
	v_pk_mul_f32 v[180:181], v[188:189], v[180:181]
	v_mov_b32_e32 v188, v182
	v_mov_b32_e32 v189, v186
	v_pk_mul_f32 v[190:191], v[190:191], v[190:191]
	v_add_f32_e32 v0, v178, v179
	v_pk_fma_f32 v[188:189], v[188:189], v[188:189], v[190:191]
	v_mov_b32_e32 v190, v180
	v_mov_b32_e32 v191, v184
	v_pk_fma_f32 v[188:189], v[190:191], v[190:191], v[188:189]
	v_mov_b32_e32 v190, v181
	v_mov_b32_e32 v191, v185
	v_pk_fma_f32 v[188:189], v[190:191], v[190:191], v[188:189]
	s_nop 0
	v_add_f32_e32 v0, v189, v0
	v_add_f32_e32 v0, v188, v0
	v_mov_b32_e32 v3, v0
	s_nop 1
	v_permlane16_swap_b32 v3, v0
	s_nop 0
	v_add_f32_e32 v0, v0, v3
	v_mov_b32_e32 v3, v0
	s_nop 1
	v_permlane32_swap_b32 v3, v0
	s_nop 0
	v_add_f32_e32 v0, v0, v3
	v_fmamk_f32 v0, v0, 0x3c800000, v246
	v_cmp_gt_f32_e64 s[40:41], s22, v0
	v_mul_f32_e32 v3, 0x4b800000, v0
	s_nop 0
	v_cndmask_b32_e64 v0, v0, v3, s[40:41]
	v_rsq_f32_e32 v0, v0
	s_nop 0
	v_mul_f32_e32 v3, 0x45800000, v0
	v_cndmask_b32_e64 v188, v0, v3, s[40:41]
	v_pk_mul_f32 v[36:37], v[36:37], v[188:189] op_sel_hi:[1,0]
	v_pk_mul_f32 v[38:39], v[38:39], v[188:189] op_sel_hi:[1,0]
	v_pk_mul_f32 v[118:119], v[118:119], v[188:189] op_sel_hi:[1,0]
	v_pk_mul_f32 v[128:129], v[128:129], v[188:189] op_sel_hi:[1,0]
	v_cmp_gt_i32_e64 s[40:41], s2, v196
	v_pk_mul_f32 v[38:39], v[34:35], v[38:39]
	v_pk_mul_f32 v[36:37], v[32:33], v[36:37]
	v_pk_mul_f32 v[192:193], v[30:31], v[128:129]
	v_pk_mul_f32 v[194:195], v[28:29], v[118:119]
	s_and_saveexec_b64 s[2:3], s[40:41]
	s_cbranch_execz .LBB0_290
	s_and_b32 s30, s4, 0x7c0
	v_add_u32_e32 v118, s30, v225
	ds_read_b128 v[208:211], v118
	v_add_u32_e32 v118, s30, v225
	ds_read_b128 v[212:215], v118 offset:4096
	s_waitcnt lgkmcnt(1)
	v_pk_mul_f32 v[118:119], v[192:193], v[210:211]
	v_pk_mul_f32 v[128:129], v[194:195], v[208:209]
	v_pk_mul_f32 v[178:179], v[38:39], v[210:211]
	v_pk_mul_f32 v[190:191], v[36:37], v[208:209]
	s_waitcnt lgkmcnt(0)
	v_pk_fma_f32 v[38:39], v[38:39], v[214:215], v[118:119] neg_lo:[0,0,1] neg_hi:[0,0,1]
	v_pk_fma_f32 v[36:37], v[36:37], v[212:213], v[128:129] neg_lo:[0,0,1] neg_hi:[0,0,1]
	v_pk_fma_f32 v[192:193], v[192:193], v[214:215], v[178:179]
	v_pk_fma_f32 v[194:195], v[194:195], v[212:213], v[190:191]

; __device__ __forceinline__ unsigned pk2(float lo, float hi) { f32x2_t v = {lo, hi}; bf16x2_t b = __builtin_convertvector(v, bf16x2_t); return __builtin_bit_cast(unsigned, b); }
; __device__ __forceinline__ float shx(float v, int m, int lane) { return __int_as_float(__builtin_amdgcn_ds_bpermute((lane ^ m) << 2, __float_as_int(v))); }
;     __device__ __forceinline__ void operator()(const pg8::i32x4 (&acc)[2][2][4][2], const Unit& u, int wr, int wc, int fr, int fq) const {
;     ...
; #pragma unroll
;             for (int ai = 0; ai < 2; ++ai)
; #pragma unroll
;                 for (int m = 0; m < 4; ++m) {
;                     const int row = u.pm * 256 + ai * 128 + wr * 64 + m * 16 + fr;
;                     float ss = 0.f; const float sa = sah[row]; f32x4 xf[2][2];
; #pragma unroll
;                     for (int bj = 0; bj < 2; ++bj)
; #pragma unroll
;                         for (int n = 0; n < 2; ++n) { f32x4 x;
; #pragma unroll
;                             for (int i = 0; i < 4; ++i) x[i] = (float)acc[ai][bj][m][n][i] * (sa * swv[bj][n][i]);
;                             xf[bj][n] = x; ss += x[0] * x[0] + x[1] * x[1] + x[2] * x[2] + x[3] * x[3]; }
;                     { const int ln = fq * 16 + fr; ss += shx(ss, 16, ln); ss += shx(ss, 32, ln); }
;                     const float rstd = rsqrtf(ss * (1.f / 64.f) + EPS);
;                     const bool lat = row < NL; const int tok = row & 2047;
; #pragma unroll
;                     for (int bj = 0; bj < 2; ++bj) {
;                         f32x4 x1 = xf[bj][0] * rstd * w[bj][0], x2 = xf[bj][1] * rstd * w[bj][1];
;                         if (lat) { const int pos = bj ? (tok & 63) : (tok >> 6); const f32x4 c = *(const f32x4*)(ropec + pos * 16 + 4 * fq), s = *(const f32x4*)(ropes + pos * 16 + 4 * fq);
;                             const f32x4 o1 = x1 * c - x2 * s, o2 = x1 * s + x2 * c; x1 = o1; x2 = o2; }
;                         x1 = x1 * osc; x2 = x2 * osc;
;                         bf16_t* p = base + (size_t)row * 512 + 64 * hg + 32 * bj + 4 * fq;
;                         *(u32x2*)p = (u32x2){pk2(x1[0], x1[1]), pk2(x1[2], x1[3])};
;                         *(u32x2*)(p + 16) = (u32x2){pk2(x2[0], x2[1]), pk2(x2[2], x2[3])};
;                     }
.LBB0_292:
	s_or_b64 exec, exec, s[2:3]
	v_mov_b32_e32 v119, v118
	v_mov_b32_e32 v182, v118
	v_mov_b32_e32 v183, v118
	v_pk_mul_f32 v[38:39], v[182:183], v[38:39]
	v_pk_mul_f32 v[36:37], v[118:119], v[36:37]
	v_pk_mul_f32 v[178:179], v[182:183], v[180:181]
	v_pk_mul_f32 v[180:181], v[118:119], v[184:185]
	v_cvt_pk_bf16_f32 v36, v36, v37
	v_cvt_pk_bf16_f32 v37, v38, v39
	global_store_dwordx2 v[190:191], v[36:37], off offset:64
	v_cvt_pk_bf16_f32 v36, v180, v181
	v_or_b32_e32 v180, 16, v196
	v_cvt_pk_bf16_f32 v37, v178, v179
	v_ashrrev_i32_e32 v181, 31, v180
	global_store_dwordx2 v[190:191], v[36:37], off offset:96
	v_lshl_add_u64 v[36:37], v[180:181], 2, s[44:45]
	v_mov_b32_e32 v0, v217
	s_mov_b32 s2, 0x8000
	v_pk_mul_f32 v[38:39], v[18:19], v[0:1] op_sel_hi:[1,0]
	v_pk_mul_f32 v[36:37], v[16:17], v[0:1] op_sel_hi:[1,0]
	v_pk_mul_f32 v[38:39], v[38:39], v[174:175]
	v_pk_mul_f32 v[174:175], v[12:13], v[0:1] op_sel_hi:[1,0]
	v_pk_mul_f32 v[36:37], v[36:37], v[176:177]
	v_pk_mul_f32 v[172:173], v[174:175], v[172:173]
	v_pk_mul_f32 v[174:175], v[14:15], v[0:1] op_sel_hi:[1,0]
	v_mov_b32_e32 v176, v37
	v_mov_b32_e32 v177, v173
	v_pk_mul_f32 v[170:171], v[174:175], v[170:171]
	v_mov_b32_e32 v174, v36
	v_mov_b32_e32 v175, v172
	v_pk_mul_f32 v[176:177], v[176:177], v[176:177]
	s_nop 0
	v_pk_fma_f32 v[174:175], v[174:175], v[174:175], v[176:177]
	v_mov_b32_e32 v176, v38
	v_mov_b32_e32 v177, v170
	v_pk_fma_f32 v[174:175], v[176:177], v[176:177], v[174:175]
	v_mov_b32_e32 v176, v39
	v_mov_b32_e32 v177, v171
	v_pk_fma_f32 v[174:175], v[176:177], v[176:177], v[174:175]
	v_pk_mul_f32 v[176:177], v[8:9], v[0:1] op_sel_hi:[1,0]
	s_nop 0
	v_pk_mul_f32 v[168:169], v[176:177], v[168:169]
	v_pk_mul_f32 v[176:177], v[10:11], v[0:1] op_sel_hi:[1,0]
	v_mov_b32_e32 v179, v169
	v_pk_mul_f32 v[142:143], v[176:177], v[142:143]
	v_pk_mul_f32 v[176:177], v[4:5], v[0:1] op_sel_hi:[1,0]
	s_nop 0
	v_pk_mul_f32 v[140:141], v[176:177], v[140:141]
	v_pk_mul_f32 v[176:177], v[6:7], v[0:1] op_sel_hi:[1,0]
	v_mov_b32_e32 v178, v141
	v_pk_mul_f32 v[138:139], v[176:177], v[138:139]
	v_mov_b32_e32 v176, v140
	v_mov_b32_e32 v177, v168
	v_pk_mul_f32 v[178:179], v[178:179], v[178:179]
	v_add_f32_e32 v0, v174, v175
	v_pk_fma_f32 v[176:177], v[176:177], v[176:177], v[178:179]
	v_mov_b32_e32 v178, v138
	v_mov_b32_e32 v179, v142
	v_pk_fma_f32 v[176:177], v[178:179], v[178:179], v[176:177]
	v_mov_b32_e32 v178, v139
	v_mov_b32_e32 v179, v143
	v_pk_fma_f32 v[176:177], v[178:179], v[178:179], v[176:177]
	s_nop 0
	v_add_f32_e32 v0, v177, v0
	v_add_f32_e32 v0, v176, v0
	v_mov_b32_e32 v3, v0
	s_nop 1
	v_permlane16_swap_b32 v3, v0
	s_nop 0
	v_add_f32_e32 v0, v0, v3
	v_mov_b32_e32 v3, v0
	s_nop 1
	v_permlane32_swap_b32 v3, v0
	s_nop 0
	v_add_f32_e32 v0, v0, v3
	v_fmamk_f32 v0, v0, 0x3c800000, v246
	v_cmp_gt_f32_e32 vcc, s22, v0
	v_mul_f32_e32 v3, 0x4b800000, v0
	s_nop 0
	v_cndmask_b32_e32 v0, v0, v3, vcc
	v_rsq_f32_e32 v0, v0
	s_nop 0
	v_mul_f32_e32 v3, 0x45800000, v0
	v_cndmask_b32_e32 v174, v0, v3, vcc
	v_pk_mul_f32 v[36:37], v[36:37], v[174:175] op_sel_hi:[1,0]
	v_pk_mul_f32 v[38:39], v[38:39], v[174:175] op_sel_hi:[1,0]
	v_pk_mul_f32 v[176:177], v[172:173], v[174:175] op_sel_hi:[1,0]
	v_pk_mul_f32 v[170:171], v[170:171], v[174:175] op_sel_hi:[1,0]
	v_cmp_gt_i32_e32 vcc, s2, v180
	v_pk_mul_f32 v[38:39], v[34:35], v[38:39]
	v_pk_mul_f32 v[36:37], v[32:33], v[36:37]
	v_pk_mul_f32 v[172:173], v[30:31], v[170:171]
	v_pk_mul_f32 v[176:177], v[28:29], v[176:177]
	s_and_saveexec_b64 s[2:3], vcc
	s_cbranch_execz .LBB0_294
	s_and_b32 s30, s4, 0x7c0
	v_add_u32_e32 v170, s30, v225
	ds_read_b128 v[184:187], v170
	v_add_u32_e32 v170, s30, v225
	ds_read_b128 v[188:191], v170 offset:4096
	s_waitcnt lgkmcnt(1)
	v_pk_mul_f32 v[170:171], v[172:173], v[186:187]
	v_pk_mul_f32 v[178:179], v[176:177], v[184:185]
	v_pk_mul_f32 v[186:187], v[38:39], v[186:187]
	v_pk_mul_f32 v[184:185], v[36:37], v[184:185]
	s_waitcnt lgkmcnt(0)
	v_pk_fma_f32 v[38:39], v[38:39], v[190:191], v[170:171] neg_lo:[0,0,1] neg_hi:[0,0,1]
	v_pk_fma_f32 v[36:37], v[36:37], v[188:189], v[178:179] neg_lo:[0,0,1] neg_hi:[0,0,1]
	v_pk_fma_f32 v[172:173], v[172:173], v[190:191], v[186:187]
	v_pk_fma_f32 v[176:177], v[176:177], v[188:189], v[184:185]

; __device__ __forceinline__ unsigned pk2(float lo, float hi) { f32x2_t v = {lo, hi}; bf16x2_t b = __builtin_convertvector(v, bf16x2_t); return __builtin_bit_cast(unsigned, b); }
; __device__ __forceinline__ float shx(float v, int m, int lane) { return __int_as_float(__builtin_amdgcn_ds_bpermute((lane ^ m) << 2, __float_as_int(v))); }
;     __device__ __forceinline__ void operator()(const pg8::i32x4 (&acc)[2][2][4][2], const Unit& u, int wr, int wc, int fr, int fq) const {
;     ...
; #pragma unroll
;             for (int ai = 0; ai < 2; ++ai)
; #pragma unroll
;                 for (int m = 0; m < 4; ++m) {
;                     const int row = u.pm * 256 + ai * 128 + wr * 64 + m * 16 + fr;
;                     float ss = 0.f; const float sa = sah[row]; f32x4 xf[2][2];
; #pragma unroll
;                     for (int bj = 0; bj < 2; ++bj)
; #pragma unroll
;                         for (int n = 0; n < 2; ++n) { f32x4 x;
; #pragma unroll
;                             for (int i = 0; i < 4; ++i) x[i] = (float)acc[ai][bj][m][n][i] * (sa * swv[bj][n][i]);
;                             xf[bj][n] = x; ss += x[0] * x[0] + x[1] * x[1] + x[2] * x[2] + x[3] * x[3]; }
;                     { const int ln = fq * 16 + fr; ss += shx(ss, 16, ln); ss += shx(ss, 32, ln); }
;                     const float rstd = rsqrtf(ss * (1.f / 64.f) + EPS);
;                     const bool lat = row < NL; const int tok = row & 2047;
; #pragma unroll
;                     for (int bj = 0; bj < 2; ++bj) {
;                         f32x4 x1 = xf[bj][0] * rstd * w[bj][0], x2 = xf[bj][1] * rstd * w[bj][1];
;                         if (lat) { const int pos = bj ? (tok & 63) : (tok >> 6); const f32x4 c = *(const f32x4*)(ropec + pos * 16 + 4 * fq), s = *(const f32x4*)(ropes + pos * 16 + 4 * fq);
;                             const f32x4 o1 = x1 * c - x2 * s, o2 = x1 * s + x2 * c; x1 = o1; x2 = o2; }
;                         x1 = x1 * osc; x2 = x2 * osc;
;                         bf16_t* p = base + (size_t)row * 512 + 64 * hg + 32 * bj + 4 * fq;
;                         *(u32x2*)p = (u32x2){pk2(x1[0], x1[1]), pk2(x1[2], x1[3])};
;                         *(u32x2*)(p + 16) = (u32x2){pk2(x2[0], x2[1]), pk2(x2[2], x2[3])};
;                     }
.LBB0_296:
	s_or_b64 exec, exec, s[2:3]
	v_mov_b32_e32 v140, v118
	v_mov_b32_e32 v141, v118
	v_pk_mul_f32 v[38:39], v[140:141], v[38:39]
	v_pk_mul_f32 v[36:37], v[118:119], v[36:37]
	v_pk_mul_f32 v[138:139], v[140:141], v[138:139]
	v_cvt_pk_bf16_f32 v36, v36, v37
	v_cvt_pk_bf16_f32 v37, v38, v39
	v_pk_mul_f32 v[142:143], v[118:119], v[142:143]
	global_store_dwordx2 v[170:171], v[36:37], off offset:64
	v_cvt_pk_bf16_f32 v37, v138, v139
	v_or_b32_e32 v138, 32, v196
	v_cvt_pk_bf16_f32 v36, v142, v143
	v_ashrrev_i32_e32 v139, 31, v138
	global_store_dwordx2 v[170:171], v[36:37], off offset:96
	v_lshl_add_u64 v[36:37], v[138:139], 2, s[44:45]
	v_mov_b32_e32 v0, v218
	s_mov_b32 s2, 0x8000
	v_pk_mul_f32 v[38:39], v[18:19], v[0:1] op_sel_hi:[1,0]
	v_pk_mul_f32 v[36:37], v[16:17], v[0:1] op_sel_hi:[1,0]
	v_pk_mul_f32 v[38:39], v[38:39], v[134:135]
	v_pk_mul_f32 v[134:135], v[12:13], v[0:1] op_sel_hi:[1,0]
	v_pk_mul_f32 v[36:37], v[36:37], v[136:137]
	v_pk_mul_f32 v[132:133], v[134:135], v[132:133]
	v_pk_mul_f32 v[134:135], v[14:15], v[0:1] op_sel_hi:[1,0]
	v_mov_b32_e32 v136, v37
	v_mov_b32_e32 v137, v133
	v_pk_mul_f32 v[130:131], v[134:135], v[130:131]
	v_mov_b32_e32 v134, v36
	v_mov_b32_e32 v135, v132
	v_pk_mul_f32 v[136:137], v[136:137], v[136:137]
	s_nop 0
	v_pk_fma_f32 v[134:135], v[134:135], v[134:135], v[136:137]
	v_mov_b32_e32 v136, v38
	v_mov_b32_e32 v137, v130
	v_pk_fma_f32 v[134:135], v[136:137], v[136:137], v[134:135]
	v_mov_b32_e32 v136, v39
	v_mov_b32_e32 v137, v131
	v_pk_fma_f32 v[134:135], v[136:137], v[136:137], v[134:135]
	v_pk_mul_f32 v[136:137], v[8:9], v[0:1] op_sel_hi:[1,0]
	s_nop 0
	v_pk_mul_f32 v[126:127], v[136:137], v[126:127]
	v_pk_mul_f32 v[136:137], v[10:11], v[0:1] op_sel_hi:[1,0]
	v_mov_b32_e32 v143, v127
	v_pk_mul_f32 v[124:125], v[136:137], v[124:125]
	v_pk_mul_f32 v[136:137], v[4:5], v[0:1] op_sel_hi:[1,0]
	s_nop 0
	v_pk_mul_f32 v[122:123], v[136:137], v[122:123]
	v_pk_mul_f32 v[136:137], v[6:7], v[0:1] op_sel_hi:[1,0]
	v_mov_b32_e32 v142, v123
	v_pk_mul_f32 v[120:121], v[136:137], v[120:121]
	v_mov_b32_e32 v136, v122
	v_mov_b32_e32 v137, v126
	v_pk_mul_f32 v[142:143], v[142:143], v[142:143]
	v_add_f32_e32 v0, v134, v135
	v_pk_fma_f32 v[136:137], v[136:137], v[136:137], v[142:143]
	v_mov_b32_e32 v142, v120
	v_mov_b32_e32 v143, v124
	v_pk_fma_f32 v[136:137], v[142:143], v[142:143], v[136:137]
	v_mov_b32_e32 v142, v121
	v_mov_b32_e32 v143, v125
	v_pk_fma_f32 v[136:137], v[142:143], v[142:143], v[136:137]
	s_nop 0
	v_add_f32_e32 v0, v137, v0
	v_add_f32_e32 v0, v136, v0
	v_mov_b32_e32 v3, v0
	s_nop 1
	v_permlane16_swap_b32 v3, v0
	s_nop 0
	v_add_f32_e32 v0, v0, v3
	v_mov_b32_e32 v3, v0
	s_nop 1
	v_permlane32_swap_b32 v3, v0
	s_nop 0
	v_add_f32_e32 v0, v0, v3
	v_fmamk_f32 v0, v0, 0x3c800000, v246
	v_cmp_gt_f32_e32 vcc, s22, v0
	v_mul_f32_e32 v3, 0x4b800000, v0
	s_nop 0
	v_cndmask_b32_e32 v0, v0, v3, vcc
	v_rsq_f32_e32 v0, v0
	s_nop 0
	v_mul_f32_e32 v3, 0x45800000, v0
	v_cndmask_b32_e32 v134, v0, v3, vcc
	v_pk_mul_f32 v[36:37], v[36:37], v[134:135] op_sel_hi:[1,0]
	v_pk_mul_f32 v[38:39], v[38:39], v[134:135] op_sel_hi:[1,0]
	v_pk_mul_f32 v[136:137], v[132:133], v[134:135] op_sel_hi:[1,0]
	v_pk_mul_f32 v[130:131], v[130:131], v[134:135] op_sel_hi:[1,0]
	v_cmp_gt_i32_e32 vcc, s2, v138
	v_pk_mul_f32 v[38:39], v[34:35], v[38:39]
	v_pk_mul_f32 v[36:37], v[32:33], v[36:37]
	v_pk_mul_f32 v[132:133], v[30:31], v[130:131]
	v_pk_mul_f32 v[136:137], v[28:29], v[136:137]
	s_and_saveexec_b64 s[2:3], vcc
	s_cbranch_execz .LBB0_298
	s_and_b32 s30, s4, 0x7c0
	v_add_u32_e32 v130, s30, v225
	ds_read_b128 v[168:171], v130
	v_add_u32_e32 v130, s30, v225
	ds_read_b128 v[172:175], v130 offset:4096
	s_waitcnt lgkmcnt(1)
	v_pk_mul_f32 v[130:131], v[132:133], v[170:171]
	v_pk_mul_f32 v[142:143], v[136:137], v[168:169]
	v_pk_mul_f32 v[170:171], v[38:39], v[170:171]
	v_pk_mul_f32 v[168:169], v[36:37], v[168:169]
	s_waitcnt lgkmcnt(0)
	v_pk_fma_f32 v[38:39], v[38:39], v[174:175], v[130:131] neg_lo:[0,0,1] neg_hi:[0,0,1]
	v_pk_fma_f32 v[36:37], v[36:37], v[172:173], v[142:143] neg_lo:[0,0,1] neg_hi:[0,0,1]
	v_pk_fma_f32 v[132:133], v[132:133], v[174:175], v[170:171]
	v_pk_fma_f32 v[136:137], v[136:137], v[172:173], v[168:169]

; __device__ __forceinline__ unsigned pk2(float lo, float hi) { f32x2_t v = {lo, hi}; bf16x2_t b = __builtin_convertvector(v, bf16x2_t); return __builtin_bit_cast(unsigned, b); }
; __device__ __forceinline__ float shx(float v, int m, int lane) { return __int_as_float(__builtin_amdgcn_ds_bpermute((lane ^ m) << 2, __float_as_int(v))); }
;     __device__ __forceinline__ void operator()(const pg8::i32x4 (&acc)[2][2][4][2], const Unit& u, int wr, int wc, int fr, int fq) const {
;     ...
; #pragma unroll
;             for (int ai = 0; ai < 2; ++ai)
; #pragma unroll
;                 for (int m = 0; m < 4; ++m) {
;                     const int row = u.pm * 256 + ai * 128 + wr * 64 + m * 16 + fr;
;                     float ss = 0.f; const float sa = sah[row]; f32x4 xf[2][2];
; #pragma unroll
;                     for (int bj = 0; bj < 2; ++bj)
; #pragma unroll
;                         for (int n = 0; n < 2; ++n) { f32x4 x;
; #pragma unroll
;                             for (int i = 0; i < 4; ++i) x[i] = (float)acc[ai][bj][m][n][i] * (sa * swv[bj][n][i]);
;                             xf[bj][n] = x; ss += x[0] * x[0] + x[1] * x[1] + x[2] * x[2] + x[3] * x[3]; }
;                     { const int ln = fq * 16 + fr; ss += shx(ss, 16, ln); ss += shx(ss, 32, ln); }
;                     const float rstd = rsqrtf(ss * (1.f / 64.f) + EPS);
;                     const bool lat = row < NL; const int tok = row & 2047;
; #pragma unroll
;                     for (int bj = 0; bj < 2; ++bj) {
;                         f32x4 x1 = xf[bj][0] * rstd * w[bj][0], x2 = xf[bj][1] * rstd * w[bj][1];
;                         if (lat) { const int pos = bj ? (tok & 63) : (tok >> 6); const f32x4 c = *(const f32x4*)(ropec + pos * 16 + 4 * fq), s = *(const f32x4*)(ropes + pos * 16 + 4 * fq);
;                             const f32x4 o1 = x1 * c - x2 * s, o2 = x1 * s + x2 * c; x1 = o1; x2 = o2; }
;                         x1 = x1 * osc; x2 = x2 * osc;
;                         bf16_t* p = base + (size_t)row * 512 + 64 * hg + 32 * bj + 4 * fq;
;                         *(u32x2*)p = (u32x2){pk2(x1[0], x1[1]), pk2(x1[2], x1[3])};
;                         *(u32x2*)(p + 16) = (u32x2){pk2(x2[0], x2[1]), pk2(x2[2], x2[3])};
;                     }
.LBB0_300:
	s_or_b64 exec, exec, s[2:3]
	v_mov_b32_e32 v122, v118
	v_mov_b32_e32 v123, v118
	v_pk_mul_f32 v[38:39], v[122:123], v[38:39]
	v_pk_mul_f32 v[36:37], v[118:119], v[36:37]
	v_pk_mul_f32 v[120:121], v[122:123], v[120:121]
	v_cvt_pk_bf16_f32 v36, v36, v37
	v_cvt_pk_bf16_f32 v37, v38, v39
	v_pk_mul_f32 v[124:125], v[118:119], v[124:125]
	global_store_dwordx2 v[130:131], v[36:37], off offset:64
	v_cvt_pk_bf16_f32 v37, v120, v121
	v_or_b32_e32 v120, 48, v196
	v_cvt_pk_bf16_f32 v36, v124, v125
	v_ashrrev_i32_e32 v121, 31, v120
	global_store_dwordx2 v[130:131], v[36:37], off offset:96
	v_lshl_add_u64 v[36:37], v[120:121], 2, s[44:45]
	v_mov_b32_e32 v0, v219
	s_mov_b32 s2, 0x8000
	v_pk_mul_f32 v[38:39], v[18:19], v[0:1] op_sel_hi:[1,0]
	v_pk_mul_f32 v[36:37], v[16:17], v[0:1] op_sel_hi:[1,0]
	v_pk_mul_f32 v[38:39], v[38:39], v[114:115]
	v_pk_mul_f32 v[114:115], v[12:13], v[0:1] op_sel_hi:[1,0]
	v_pk_mul_f32 v[36:37], v[36:37], v[116:117]
	v_pk_mul_f32 v[112:113], v[114:115], v[112:113]
	v_pk_mul_f32 v[114:115], v[14:15], v[0:1] op_sel_hi:[1,0]
	v_mov_b32_e32 v116, v37
	v_mov_b32_e32 v117, v113
	v_pk_mul_f32 v[110:111], v[114:115], v[110:111]
	v_mov_b32_e32 v114, v36
	v_mov_b32_e32 v115, v112
	v_pk_mul_f32 v[116:117], v[116:117], v[116:117]
	s_nop 0
	v_pk_fma_f32 v[114:115], v[114:115], v[114:115], v[116:117]
	v_mov_b32_e32 v116, v38
	v_mov_b32_e32 v117, v110
	v_pk_fma_f32 v[114:115], v[116:117], v[116:117], v[114:115]
	v_mov_b32_e32 v116, v39
	v_mov_b32_e32 v117, v111
	v_pk_fma_f32 v[114:115], v[116:117], v[116:117], v[114:115]
	v_pk_mul_f32 v[116:117], v[8:9], v[0:1] op_sel_hi:[1,0]
	s_nop 0
	v_pk_mul_f32 v[108:109], v[116:117], v[108:109]
	v_pk_mul_f32 v[116:117], v[10:11], v[0:1] op_sel_hi:[1,0]
	v_mov_b32_e32 v125, v109
	v_pk_mul_f32 v[106:107], v[116:117], v[106:107]
	v_pk_mul_f32 v[116:117], v[4:5], v[0:1] op_sel_hi:[1,0]
	s_nop 0
	v_pk_mul_f32 v[104:105], v[116:117], v[104:105]
	v_pk_mul_f32 v[116:117], v[6:7], v[0:1] op_sel_hi:[1,0]
	v_mov_b32_e32 v124, v105
	v_pk_mul_f32 v[102:103], v[116:117], v[102:103]
	v_mov_b32_e32 v116, v104
	v_mov_b32_e32 v117, v108
	v_pk_mul_f32 v[124:125], v[124:125], v[124:125]
	v_add_f32_e32 v0, v114, v115
	v_pk_fma_f32 v[116:117], v[116:117], v[116:117], v[124:125]
	v_mov_b32_e32 v124, v102
	v_mov_b32_e32 v125, v106
	v_pk_fma_f32 v[116:117], v[124:125], v[124:125], v[116:117]
	v_mov_b32_e32 v124, v103
	v_mov_b32_e32 v125, v107
	v_pk_fma_f32 v[116:117], v[124:125], v[124:125], v[116:117]
	s_nop 0
	v_add_f32_e32 v0, v117, v0
	v_add_f32_e32 v0, v116, v0
	v_mov_b32_e32 v3, v0
	s_nop 1
	v_permlane16_swap_b32 v3, v0
	s_nop 0
	v_add_f32_e32 v0, v0, v3
	v_mov_b32_e32 v3, v0
	s_nop 1
	v_permlane32_swap_b32 v3, v0
	s_nop 0
	v_add_f32_e32 v0, v0, v3
	v_fmamk_f32 v0, v0, 0x3c800000, v246
	v_cmp_gt_f32_e32 vcc, s22, v0
	v_mul_f32_e32 v3, 0x4b800000, v0
	s_nop 0
	v_cndmask_b32_e32 v0, v0, v3, vcc
	v_rsq_f32_e32 v0, v0
	s_nop 0
	v_mul_f32_e32 v3, 0x45800000, v0
	v_cndmask_b32_e32 v114, v0, v3, vcc
	v_pk_mul_f32 v[36:37], v[36:37], v[114:115] op_sel_hi:[1,0]
	v_pk_mul_f32 v[38:39], v[38:39], v[114:115] op_sel_hi:[1,0]
	v_pk_mul_f32 v[116:117], v[112:113], v[114:115] op_sel_hi:[1,0]
	v_pk_mul_f32 v[110:111], v[110:111], v[114:115] op_sel_hi:[1,0]
	v_cmp_gt_i32_e32 vcc, s2, v120
	v_pk_mul_f32 v[38:39], v[34:35], v[38:39]
	v_pk_mul_f32 v[36:37], v[32:33], v[36:37]
	v_pk_mul_f32 v[112:113], v[30:31], v[110:111]
	v_pk_mul_f32 v[116:117], v[28:29], v[116:117]
	s_and_saveexec_b64 s[2:3], vcc
	s_cbranch_execz .LBB0_302
	s_and_b32 s30, s4, 0x7c0
	v_add_u32_e32 v110, s30, v225
	ds_read_b128 v[124:127], v110
	v_add_u32_e32 v110, s30, v225
	ds_read_b128 v[130:133], v110 offset:4096
	s_waitcnt lgkmcnt(1)
	v_pk_mul_f32 v[110:111], v[112:113], v[126:127]
	v_pk_mul_f32 v[134:135], v[116:117], v[124:125]
	v_pk_mul_f32 v[126:127], v[38:39], v[126:127]
	v_pk_mul_f32 v[124:125], v[36:37], v[124:125]
	s_waitcnt lgkmcnt(0)
	v_pk_fma_f32 v[38:39], v[38:39], v[132:133], v[110:111] neg_lo:[0,0,1] neg_hi:[0,0,1]
	v_pk_fma_f32 v[36:37], v[36:37], v[130:131], v[134:135] neg_lo:[0,0,1] neg_hi:[0,0,1]
	v_pk_fma_f32 v[112:113], v[112:113], v[132:133], v[126:127]
	v_pk_fma_f32 v[116:117], v[116:117], v[130:131], v[124:125]

; __device__ __forceinline__ unsigned pk2(float lo, float hi) { f32x2_t v = {lo, hi}; bf16x2_t b = __builtin_convertvector(v, bf16x2_t); return __builtin_bit_cast(unsigned, b); }
; __device__ __forceinline__ float shx(float v, int m, int lane) { return __int_as_float(__builtin_amdgcn_ds_bpermute((lane ^ m) << 2, __float_as_int(v))); }
;     __device__ __forceinline__ void operator()(const pg8::i32x4 (&acc)[2][2][4][2], const Unit& u, int wr, int wc, int fr, int fq) const {
;     ...
; #pragma unroll
;             for (int ai = 0; ai < 2; ++ai)
; #pragma unroll
;                 for (int m = 0; m < 4; ++m) {
;                     const int row = u.pm * 256 + ai * 128 + wr * 64 + m * 16 + fr;
;                     float ss = 0.f; const float sa = sah[row]; f32x4 xf[2][2];
; #pragma unroll
;                     for (int bj = 0; bj < 2; ++bj)
; #pragma unroll
;                         for (int n = 0; n < 2; ++n) { f32x4 x;
; #pragma unroll
;                             for (int i = 0; i < 4; ++i) x[i] = (float)acc[ai][bj][m][n][i] * (sa * swv[bj][n][i]);
;                             xf[bj][n] = x; ss += x[0] * x[0] + x[1] * x[1] + x[2] * x[2] + x[3] * x[3]; }
;                     { const int ln = fq * 16 + fr; ss += shx(ss, 16, ln); ss += shx(ss, 32, ln); }
;                     const float rstd = rsqrtf(ss * (1.f / 64.f) + EPS);
;                     const bool lat = row < NL; const int tok = row & 2047;
; #pragma unroll
;                     for (int bj = 0; bj < 2; ++bj) {
;                         f32x4 x1 = xf[bj][0] * rstd * w[bj][0], x2 = xf[bj][1] * rstd * w[bj][1];
;                         if (lat) { const int pos = bj ? (tok & 63) : (tok >> 6); const f32x4 c = *(const f32x4*)(ropec + pos * 16 + 4 * fq), s = *(const f32x4*)(ropes + pos * 16 + 4 * fq);
;                             const f32x4 o1 = x1 * c - x2 * s, o2 = x1 * s + x2 * c; x1 = o1; x2 = o2; }
;                         x1 = x1 * osc; x2 = x2 * osc;
;                         bf16_t* p = base + (size_t)row * 512 + 64 * hg + 32 * bj + 4 * fq;
;                         *(u32x2*)p = (u32x2){pk2(x1[0], x1[1]), pk2(x1[2], x1[3])};
;                         *(u32x2*)(p + 16) = (u32x2){pk2(x2[0], x2[1]), pk2(x2[2], x2[3])};
;                     }
.LBB0_304:
	s_or_b64 exec, exec, s[2:3]
	v_mov_b32_e32 v104, v118
	v_mov_b32_e32 v105, v118
	v_pk_mul_f32 v[38:39], v[104:105], v[38:39]
	v_pk_mul_f32 v[36:37], v[118:119], v[36:37]
	v_pk_mul_f32 v[102:103], v[104:105], v[102:103]
	v_cvt_pk_bf16_f32 v36, v36, v37
	v_cvt_pk_bf16_f32 v37, v38, v39
	s_addk_i32 s4, 0x80
	v_pk_mul_f32 v[106:107], v[118:119], v[106:107]
	global_store_dwordx2 v[110:111], v[36:37], off offset:64
	v_cvt_pk_bf16_f32 v37, v102, v103
	v_or_b32_e32 v102, s4, v198
	v_cvt_pk_bf16_f32 v36, v106, v107
	v_ashrrev_i32_e32 v103, 31, v102
	global_store_dwordx2 v[110:111], v[36:37], off offset:96
	v_lshl_add_u64 v[36:37], v[102:103], 2, s[44:45]
	v_mov_b32_e32 v0, v220
	s_mov_b32 s2, 0x8000
	v_pk_mul_f32 v[38:39], v[18:19], v[0:1] op_sel_hi:[1,0]
	v_pk_mul_f32 v[36:37], v[16:17], v[0:1] op_sel_hi:[1,0]
	v_pk_mul_f32 v[38:39], v[38:39], v[98:99]
	v_pk_mul_f32 v[98:99], v[12:13], v[0:1] op_sel_hi:[1,0]
	v_pk_mul_f32 v[36:37], v[36:37], v[100:101]
	v_pk_mul_f32 v[96:97], v[98:99], v[96:97]
	v_pk_mul_f32 v[98:99], v[14:15], v[0:1] op_sel_hi:[1,0]
	v_mov_b32_e32 v100, v37
	v_mov_b32_e32 v101, v97
	v_pk_mul_f32 v[94:95], v[98:99], v[94:95]
	v_mov_b32_e32 v98, v36
	v_mov_b32_e32 v99, v96
	v_pk_mul_f32 v[100:101], v[100:101], v[100:101]
	s_nop 0
	v_pk_fma_f32 v[98:99], v[98:99], v[98:99], v[100:101]
	v_mov_b32_e32 v100, v38
	v_mov_b32_e32 v101, v94
	v_pk_fma_f32 v[98:99], v[100:101], v[100:101], v[98:99]
	v_mov_b32_e32 v100, v39
	v_mov_b32_e32 v101, v95
	v_pk_fma_f32 v[98:99], v[100:101], v[100:101], v[98:99]
	v_pk_mul_f32 v[100:101], v[8:9], v[0:1] op_sel_hi:[1,0]
	s_nop 0
	v_pk_mul_f32 v[92:93], v[100:101], v[92:93]
	v_pk_mul_f32 v[100:101], v[10:11], v[0:1] op_sel_hi:[1,0]
	v_mov_b32_e32 v107, v93
	v_pk_mul_f32 v[90:91], v[100:101], v[90:91]
	v_pk_mul_f32 v[100:101], v[4:5], v[0:1] op_sel_hi:[1,0]
	s_nop 0
	v_pk_mul_f32 v[88:89], v[100:101], v[88:89]
	v_pk_mul_f32 v[100:101], v[6:7], v[0:1] op_sel_hi:[1,0]
	v_mov_b32_e32 v106, v89
	v_pk_mul_f32 v[86:87], v[100:101], v[86:87]
	v_mov_b32_e32 v100, v88
	v_mov_b32_e32 v101, v92
	v_pk_mul_f32 v[106:107], v[106:107], v[106:107]
	v_add_f32_e32 v0, v98, v99
	v_pk_fma_f32 v[100:101], v[100:101], v[100:101], v[106:107]
	v_mov_b32_e32 v106, v86
	v_mov_b32_e32 v107, v90
	v_pk_fma_f32 v[100:101], v[106:107], v[106:107], v[100:101]
	v_mov_b32_e32 v106, v87
	v_mov_b32_e32 v107, v91
	v_pk_fma_f32 v[100:101], v[106:107], v[106:107], v[100:101]
	s_nop 0
	v_add_f32_e32 v0, v101, v0
	v_add_f32_e32 v0, v100, v0
	v_mov_b32_e32 v3, v0
	s_nop 1
	v_permlane16_swap_b32 v3, v0
	s_nop 0
	v_add_f32_e32 v0, v0, v3
	v_mov_b32_e32 v3, v0
	s_nop 1
	v_permlane32_swap_b32 v3, v0
	s_nop 0
	v_add_f32_e32 v0, v0, v3
	v_fmamk_f32 v0, v0, 0x3c800000, v246
	v_cmp_gt_f32_e32 vcc, s22, v0
	v_mul_f32_e32 v3, 0x4b800000, v0
	s_nop 0
	v_cndmask_b32_e32 v0, v0, v3, vcc
	v_rsq_f32_e32 v0, v0
	s_nop 0
	v_mul_f32_e32 v3, 0x45800000, v0
	v_cndmask_b32_e32 v98, v0, v3, vcc
	v_pk_mul_f32 v[36:37], v[36:37], v[98:99] op_sel_hi:[1,0]
	v_pk_mul_f32 v[38:39], v[38:39], v[98:99] op_sel_hi:[1,0]
	v_pk_mul_f32 v[100:101], v[96:97], v[98:99] op_sel_hi:[1,0]
	v_pk_mul_f32 v[94:95], v[94:95], v[98:99] op_sel_hi:[1,0]
	v_cmp_gt_i32_e32 vcc, s2, v102
	v_pk_mul_f32 v[38:39], v[34:35], v[38:39]
	v_pk_mul_f32 v[36:37], v[32:33], v[36:37]
	v_pk_mul_f32 v[96:97], v[30:31], v[94:95]
	v_pk_mul_f32 v[100:101], v[28:29], v[100:101]
	s_and_saveexec_b64 s[2:3], vcc
	s_cbranch_execz .LBB0_306
	s_and_b32 s30, s4, 0x7c0
	v_add_u32_e32 v94, s30, v225
	ds_read_b128 v[106:109], v94
	v_add_u32_e32 v94, s30, v225
	ds_read_b128 v[110:113], v94 offset:4096
	s_waitcnt lgkmcnt(1)
	v_pk_mul_f32 v[94:95], v[96:97], v[108:109]
	v_pk_mul_f32 v[114:115], v[100:101], v[106:107]
	v_pk_mul_f32 v[108:109], v[38:39], v[108:109]
	v_pk_mul_f32 v[106:107], v[36:37], v[106:107]
	s_waitcnt lgkmcnt(0)
	v_pk_fma_f32 v[38:39], v[38:39], v[112:113], v[94:95] neg_lo:[0,0,1] neg_hi:[0,0,1]
	v_pk_fma_f32 v[36:37], v[36:37], v[110:111], v[114:115] neg_lo:[0,0,1] neg_hi:[0,0,1]
	v_pk_fma_f32 v[96:97], v[96:97], v[112:113], v[108:109]
	v_pk_fma_f32 v[100:101], v[100:101], v[110:111], v[106:107]

; __device__ __forceinline__ unsigned pk2(float lo, float hi) { f32x2_t v = {lo, hi}; bf16x2_t b = __builtin_convertvector(v, bf16x2_t); return __builtin_bit_cast(unsigned, b); }
; __device__ __forceinline__ float shx(float v, int m, int lane) { return __int_as_float(__builtin_amdgcn_ds_bpermute((lane ^ m) << 2, __float_as_int(v))); }
;     __device__ __forceinline__ void operator()(const pg8::i32x4 (&acc)[2][2][4][2], const Unit& u, int wr, int wc, int fr, int fq) const {
;     ...
; #pragma unroll
;             for (int ai = 0; ai < 2; ++ai)
; #pragma unroll
;                 for (int m = 0; m < 4; ++m) {
;                     const int row = u.pm * 256 + ai * 128 + wr * 64 + m * 16 + fr;
;                     float ss = 0.f; const float sa = sah[row]; f32x4 xf[2][2];
; #pragma unroll
;                     for (int bj = 0; bj < 2; ++bj)
; #pragma unroll
;                         for (int n = 0; n < 2; ++n) { f32x4 x;
; #pragma unroll
;                             for (int i = 0; i < 4; ++i) x[i] = (float)acc[ai][bj][m][n][i] * (sa * swv[bj][n][i]);
;                             xf[bj][n] = x; ss += x[0] * x[0] + x[1] * x[1] + x[2] * x[2] + x[3] * x[3]; }
;                     { const int ln = fq * 16 + fr; ss += shx(ss, 16, ln); ss += shx(ss, 32, ln); }
;                     const float rstd = rsqrtf(ss * (1.f / 64.f) + EPS);
;                     const bool lat = row < NL; const int tok = row & 2047;
; #pragma unroll
;                     for (int bj = 0; bj < 2; ++bj) {
;                         f32x4 x1 = xf[bj][0] * rstd * w[bj][0], x2 = xf[bj][1] * rstd * w[bj][1];
;                         if (lat) { const int pos = bj ? (tok & 63) : (tok >> 6); const f32x4 c = *(const f32x4*)(ropec + pos * 16 + 4 * fq), s = *(const f32x4*)(ropes + pos * 16 + 4 * fq);
;                             const f32x4 o1 = x1 * c - x2 * s, o2 = x1 * s + x2 * c; x1 = o1; x2 = o2; }
;                         x1 = x1 * osc; x2 = x2 * osc;
;                         bf16_t* p = base + (size_t)row * 512 + 64 * hg + 32 * bj + 4 * fq;
;                         *(u32x2*)p = (u32x2){pk2(x1[0], x1[1]), pk2(x1[2], x1[3])};
;                         *(u32x2*)(p + 16) = (u32x2){pk2(x2[0], x2[1]), pk2(x2[2], x2[3])};
;                     }
.LBB0_308:
	s_or_b64 exec, exec, s[2:3]
	v_mov_b32_e32 v88, v118
	v_mov_b32_e32 v89, v118
	v_pk_mul_f32 v[38:39], v[88:89], v[38:39]
	v_pk_mul_f32 v[36:37], v[118:119], v[36:37]
	v_pk_mul_f32 v[86:87], v[88:89], v[86:87]
	v_cvt_pk_bf16_f32 v36, v36, v37
	v_cvt_pk_bf16_f32 v37, v38, v39
	v_pk_mul_f32 v[90:91], v[118:119], v[90:91]
	global_store_dwordx2 v[94:95], v[36:37], off offset:64
	v_cvt_pk_bf16_f32 v37, v86, v87
	v_or_b32_e32 v86, 16, v102
	v_cvt_pk_bf16_f32 v36, v90, v91
	v_ashrrev_i32_e32 v87, 31, v86
	global_store_dwordx2 v[94:95], v[36:37], off offset:96
	v_lshl_add_u64 v[36:37], v[86:87], 2, s[44:45]
	v_mov_b32_e32 v0, v221
	s_mov_b32 s2, 0x8000
	v_pk_mul_f32 v[38:39], v[18:19], v[0:1] op_sel_hi:[1,0]
	v_pk_mul_f32 v[36:37], v[16:17], v[0:1] op_sel_hi:[1,0]
	v_pk_mul_f32 v[38:39], v[38:39], v[82:83]
	v_pk_mul_f32 v[82:83], v[12:13], v[0:1] op_sel_hi:[1,0]
	v_pk_mul_f32 v[36:37], v[36:37], v[84:85]
	v_pk_mul_f32 v[80:81], v[82:83], v[80:81]
	v_pk_mul_f32 v[82:83], v[14:15], v[0:1] op_sel_hi:[1,0]
	v_mov_b32_e32 v84, v37
	v_mov_b32_e32 v85, v81
	v_pk_mul_f32 v[78:79], v[82:83], v[78:79]
	v_mov_b32_e32 v82, v36
	v_mov_b32_e32 v83, v80
	v_pk_mul_f32 v[84:85], v[84:85], v[84:85]
	s_nop 0
	v_pk_fma_f32 v[82:83], v[82:83], v[82:83], v[84:85]
	v_mov_b32_e32 v84, v38
	v_mov_b32_e32 v85, v78
	v_pk_fma_f32 v[82:83], v[84:85], v[84:85], v[82:83]
	v_mov_b32_e32 v84, v39
	v_mov_b32_e32 v85, v79
	v_pk_fma_f32 v[82:83], v[84:85], v[84:85], v[82:83]
	v_pk_mul_f32 v[84:85], v[8:9], v[0:1] op_sel_hi:[1,0]
	s_nop 0
	v_pk_mul_f32 v[76:77], v[84:85], v[76:77]
	v_pk_mul_f32 v[84:85], v[10:11], v[0:1] op_sel_hi:[1,0]
	v_mov_b32_e32 v91, v77
	v_pk_mul_f32 v[74:75], v[84:85], v[74:75]
	v_pk_mul_f32 v[84:85], v[4:5], v[0:1] op_sel_hi:[1,0]
	s_nop 0
	v_pk_mul_f32 v[72:73], v[84:85], v[72:73]
	v_pk_mul_f32 v[84:85], v[6:7], v[0:1] op_sel_hi:[1,0]
	v_mov_b32_e32 v90, v73
	v_pk_mul_f32 v[70:71], v[84:85], v[70:71]
	v_mov_b32_e32 v84, v72
	v_mov_b32_e32 v85, v76
	v_pk_mul_f32 v[90:91], v[90:91], v[90:91]
	v_add_f32_e32 v0, v82, v83
	v_pk_fma_f32 v[84:85], v[84:85], v[84:85], v[90:91]
	v_mov_b32_e32 v90, v70
	v_mov_b32_e32 v91, v74
	v_pk_fma_f32 v[84:85], v[90:91], v[90:91], v[84:85]
	v_mov_b32_e32 v90, v71
	v_mov_b32_e32 v91, v75
	v_pk_fma_f32 v[84:85], v[90:91], v[90:91], v[84:85]
	s_nop 0
	v_add_f32_e32 v0, v85, v0
	v_add_f32_e32 v0, v84, v0
	v_mov_b32_e32 v3, v0
	s_nop 1
	v_permlane16_swap_b32 v3, v0
	s_nop 0
	v_add_f32_e32 v0, v0, v3
	v_mov_b32_e32 v3, v0
	s_nop 1
	v_permlane32_swap_b32 v3, v0
	s_nop 0
	v_add_f32_e32 v0, v0, v3
	v_fmamk_f32 v0, v0, 0x3c800000, v246
	v_cmp_gt_f32_e32 vcc, s22, v0
	v_mul_f32_e32 v3, 0x4b800000, v0
	s_nop 0
	v_cndmask_b32_e32 v0, v0, v3, vcc
	v_rsq_f32_e32 v0, v0
	s_nop 0
	v_mul_f32_e32 v3, 0x45800000, v0
	v_cndmask_b32_e32 v82, v0, v3, vcc
	v_pk_mul_f32 v[36:37], v[36:37], v[82:83] op_sel_hi:[1,0]
	v_pk_mul_f32 v[38:39], v[38:39], v[82:83] op_sel_hi:[1,0]
	v_pk_mul_f32 v[84:85], v[80:81], v[82:83] op_sel_hi:[1,0]
	v_pk_mul_f32 v[78:79], v[78:79], v[82:83] op_sel_hi:[1,0]
	v_cmp_gt_i32_e32 vcc, s2, v86
	v_pk_mul_f32 v[38:39], v[34:35], v[38:39]
	v_pk_mul_f32 v[36:37], v[32:33], v[36:37]
	v_pk_mul_f32 v[80:81], v[30:31], v[78:79]
	v_pk_mul_f32 v[84:85], v[28:29], v[84:85]
	s_and_saveexec_b64 s[2:3], vcc
	s_cbranch_execz .LBB0_310
	s_and_b32 s30, s4, 0x7c0
	v_add_u32_e32 v78, s30, v225
	ds_read_b128 v[90:93], v78
	v_add_u32_e32 v78, s30, v225
	ds_read_b128 v[94:97], v78 offset:4096
	s_waitcnt lgkmcnt(1)
	v_pk_mul_f32 v[78:79], v[80:81], v[92:93]
	v_pk_mul_f32 v[98:99], v[84:85], v[90:91]
	v_pk_mul_f32 v[92:93], v[38:39], v[92:93]
	v_pk_mul_f32 v[90:91], v[36:37], v[90:91]
	s_waitcnt lgkmcnt(0)
	v_pk_fma_f32 v[38:39], v[38:39], v[96:97], v[78:79] neg_lo:[0,0,1] neg_hi:[0,0,1]
	v_pk_fma_f32 v[36:37], v[36:37], v[94:95], v[98:99] neg_lo:[0,0,1] neg_hi:[0,0,1]
	v_pk_fma_f32 v[80:81], v[80:81], v[96:97], v[92:93]
	v_pk_fma_f32 v[84:85], v[84:85], v[94:95], v[90:91]

; __device__ __forceinline__ unsigned pk2(float lo, float hi) { f32x2_t v = {lo, hi}; bf16x2_t b = __builtin_convertvector(v, bf16x2_t); return __builtin_bit_cast(unsigned, b); }
; __device__ __forceinline__ float shx(float v, int m, int lane) { return __int_as_float(__builtin_amdgcn_ds_bpermute((lane ^ m) << 2, __float_as_int(v))); }
;     __device__ __forceinline__ void operator()(const pg8::i32x4 (&acc)[2][2][4][2], const Unit& u, int wr, int wc, int fr, int fq) const {
;     ...
; #pragma unroll
;             for (int ai = 0; ai < 2; ++ai)
; #pragma unroll
;                 for (int m = 0; m < 4; ++m) {
;                     const int row = u.pm * 256 + ai * 128 + wr * 64 + m * 16 + fr;
;                     float ss = 0.f; const float sa = sah[row]; f32x4 xf[2][2];
; #pragma unroll
;                     for (int bj = 0; bj < 2; ++bj)
; #pragma unroll
;                         for (int n = 0; n < 2; ++n) { f32x4 x;
; #pragma unroll
;                             for (int i = 0; i < 4; ++i) x[i] = (float)acc[ai][bj][m][n][i] * (sa * swv[bj][n][i]);
;                             xf[bj][n] = x; ss += x[0] * x[0] + x[1] * x[1] + x[2] * x[2] + x[3] * x[3]; }
;                     { const int ln = fq * 16 + fr; ss += shx(ss, 16, ln); ss += shx(ss, 32, ln); }
;                     const float rstd = rsqrtf(ss * (1.f / 64.f) + EPS);
;                     const bool lat = row < NL; const int tok = row & 2047;
; #pragma unroll
;                     for (int bj = 0; bj < 2; ++bj) {
;                         f32x4 x1 = xf[bj][0] * rstd * w[bj][0], x2 = xf[bj][1] * rstd * w[bj][1];
;                         if (lat) { const int pos = bj ? (tok & 63) : (tok >> 6); const f32x4 c = *(const f32x4*)(ropec + pos * 16 + 4 * fq), s = *(const f32x4*)(ropes + pos * 16 + 4 * fq);
;                             const f32x4 o1 = x1 * c - x2 * s, o2 = x1 * s + x2 * c; x1 = o1; x2 = o2; }
;                         x1 = x1 * osc; x2 = x2 * osc;
;                         bf16_t* p = base + (size_t)row * 512 + 64 * hg + 32 * bj + 4 * fq;
;                         *(u32x2*)p = (u32x2){pk2(x1[0], x1[1]), pk2(x1[2], x1[3])};
;                         *(u32x2*)(p + 16) = (u32x2){pk2(x2[0], x2[1]), pk2(x2[2], x2[3])};
;                     }
.LBB0_312:
	s_or_b64 exec, exec, s[2:3]
	v_mov_b32_e32 v72, v118
	v_mov_b32_e32 v73, v118
	v_pk_mul_f32 v[38:39], v[72:73], v[38:39]
	v_pk_mul_f32 v[36:37], v[118:119], v[36:37]
	v_pk_mul_f32 v[70:71], v[72:73], v[70:71]
	v_cvt_pk_bf16_f32 v36, v36, v37
	v_cvt_pk_bf16_f32 v37, v38, v39
	v_pk_mul_f32 v[74:75], v[118:119], v[74:75]
	global_store_dwordx2 v[78:79], v[36:37], off offset:64
	v_cvt_pk_bf16_f32 v37, v70, v71
	v_or_b32_e32 v70, 32, v102
	v_cvt_pk_bf16_f32 v36, v74, v75
	v_ashrrev_i32_e32 v71, 31, v70
	global_store_dwordx2 v[78:79], v[36:37], off offset:96
	v_lshl_add_u64 v[36:37], v[70:71], 2, s[44:45]
	v_mov_b32_e32 v0, v222
	s_mov_b32 s2, 0x8000
	v_pk_mul_f32 v[38:39], v[18:19], v[0:1] op_sel_hi:[1,0]
	v_pk_mul_f32 v[36:37], v[16:17], v[0:1] op_sel_hi:[1,0]
	v_pk_mul_f32 v[38:39], v[38:39], v[66:67]
	v_pk_mul_f32 v[66:67], v[12:13], v[0:1] op_sel_hi:[1,0]
	v_pk_mul_f32 v[36:37], v[36:37], v[68:69]
	v_pk_mul_f32 v[64:65], v[66:67], v[64:65]
	v_pk_mul_f32 v[66:67], v[14:15], v[0:1] op_sel_hi:[1,0]
	v_mov_b32_e32 v68, v37
	v_mov_b32_e32 v69, v65
	v_pk_mul_f32 v[62:63], v[66:67], v[62:63]
	v_mov_b32_e32 v66, v36
	v_mov_b32_e32 v67, v64
	v_pk_mul_f32 v[68:69], v[68:69], v[68:69]
	s_nop 0
	v_pk_fma_f32 v[66:67], v[66:67], v[66:67], v[68:69]
	v_mov_b32_e32 v68, v38
	v_mov_b32_e32 v69, v62
	v_pk_fma_f32 v[66:67], v[68:69], v[68:69], v[66:67]
	v_mov_b32_e32 v68, v39
	v_mov_b32_e32 v69, v63
	v_pk_fma_f32 v[66:67], v[68:69], v[68:69], v[66:67]
	v_pk_mul_f32 v[68:69], v[8:9], v[0:1] op_sel_hi:[1,0]
	s_nop 0
	v_pk_mul_f32 v[60:61], v[68:69], v[60:61]
	v_pk_mul_f32 v[68:69], v[10:11], v[0:1] op_sel_hi:[1,0]
	v_mov_b32_e32 v75, v61
	v_pk_mul_f32 v[58:59], v[68:69], v[58:59]
	v_pk_mul_f32 v[68:69], v[4:5], v[0:1] op_sel_hi:[1,0]
	s_nop 0
	v_pk_mul_f32 v[56:57], v[68:69], v[56:57]
	v_pk_mul_f32 v[68:69], v[6:7], v[0:1] op_sel_hi:[1,0]
	v_mov_b32_e32 v74, v57
	v_pk_mul_f32 v[54:55], v[68:69], v[54:55]
	v_mov_b32_e32 v68, v56
	v_mov_b32_e32 v69, v60
	v_pk_mul_f32 v[74:75], v[74:75], v[74:75]
	v_add_f32_e32 v0, v66, v67
	v_pk_fma_f32 v[68:69], v[68:69], v[68:69], v[74:75]
	v_mov_b32_e32 v74, v54
	v_mov_b32_e32 v75, v58
	v_pk_fma_f32 v[68:69], v[74:75], v[74:75], v[68:69]
	v_mov_b32_e32 v74, v55
	v_mov_b32_e32 v75, v59
	v_pk_fma_f32 v[68:69], v[74:75], v[74:75], v[68:69]
	s_nop 0
	v_add_f32_e32 v0, v69, v0
	v_add_f32_e32 v0, v68, v0
	v_mov_b32_e32 v3, v0
	s_nop 1
	v_permlane16_swap_b32 v3, v0
	s_nop 0
	v_add_f32_e32 v0, v0, v3
	v_mov_b32_e32 v3, v0
	s_nop 1
	v_permlane32_swap_b32 v3, v0
	s_nop 0
	v_add_f32_e32 v0, v0, v3
	v_fmamk_f32 v0, v0, 0x3c800000, v246
	v_cmp_gt_f32_e32 vcc, s22, v0
	v_mul_f32_e32 v3, 0x4b800000, v0
	s_nop 0
	v_cndmask_b32_e32 v0, v0, v3, vcc
	v_rsq_f32_e32 v0, v0
	s_nop 0
	v_mul_f32_e32 v3, 0x45800000, v0
	v_cndmask_b32_e32 v66, v0, v3, vcc
	v_pk_mul_f32 v[36:37], v[36:37], v[66:67] op_sel_hi:[1,0]
	v_pk_mul_f32 v[38:39], v[38:39], v[66:67] op_sel_hi:[1,0]
	v_pk_mul_f32 v[68:69], v[64:65], v[66:67] op_sel_hi:[1,0]
	v_pk_mul_f32 v[62:63], v[62:63], v[66:67] op_sel_hi:[1,0]
	v_cmp_gt_i32_e32 vcc, s2, v70
	v_pk_mul_f32 v[38:39], v[34:35], v[38:39]
	v_pk_mul_f32 v[36:37], v[32:33], v[36:37]
	v_pk_mul_f32 v[64:65], v[30:31], v[62:63]
	v_pk_mul_f32 v[68:69], v[28:29], v[68:69]
	s_and_saveexec_b64 s[2:3], vcc
	s_cbranch_execz .LBB0_314
	s_and_b32 s30, s4, 0x7c0
	v_add_u32_e32 v62, s30, v225
	ds_read_b128 v[74:77], v62
	v_add_u32_e32 v62, s30, v225
	ds_read_b128 v[78:81], v62 offset:4096
	s_waitcnt lgkmcnt(1)
	v_pk_mul_f32 v[62:63], v[64:65], v[76:77]
	v_pk_mul_f32 v[82:83], v[68:69], v[74:75]
	v_pk_mul_f32 v[76:77], v[38:39], v[76:77]
	v_pk_mul_f32 v[74:75], v[36:37], v[74:75]
	s_waitcnt lgkmcnt(0)
	v_pk_fma_f32 v[38:39], v[38:39], v[80:81], v[62:63] neg_lo:[0,0,1] neg_hi:[0,0,1]
	v_pk_fma_f32 v[36:37], v[36:37], v[78:79], v[82:83] neg_lo:[0,0,1] neg_hi:[0,0,1]
	v_pk_fma_f32 v[64:65], v[64:65], v[80:81], v[76:77]
	v_pk_fma_f32 v[68:69], v[68:69], v[78:79], v[74:75]

; __device__ __forceinline__ unsigned pk2(float lo, float hi) { f32x2_t v = {lo, hi}; bf16x2_t b = __builtin_convertvector(v, bf16x2_t); return __builtin_bit_cast(unsigned, b); }
; __device__ __forceinline__ float shx(float v, int m, int lane) { return __int_as_float(__builtin_amdgcn_ds_bpermute((lane ^ m) << 2, __float_as_int(v))); }
;     __device__ __forceinline__ void operator()(const pg8::i32x4 (&acc)[2][2][4][2], const Unit& u, int wr, int wc, int fr, int fq) const {
;     ...
; #pragma unroll
;             for (int ai = 0; ai < 2; ++ai)
; #pragma unroll
;                 for (int m = 0; m < 4; ++m) {
;                     const int row = u.pm * 256 + ai * 128 + wr * 64 + m * 16 + fr;
;                     float ss = 0.f; const float sa = sah[row]; f32x4 xf[2][2];
; #pragma unroll
;                     for (int bj = 0; bj < 2; ++bj)
; #pragma unroll
;                         for (int n = 0; n < 2; ++n) { f32x4 x;
; #pragma unroll
;                             for (int i = 0; i < 4; ++i) x[i] = (float)acc[ai][bj][m][n][i] * (sa * swv[bj][n][i]);
;                             xf[bj][n] = x; ss += x[0] * x[0] + x[1] * x[1] + x[2] * x[2] + x[3] * x[3]; }
;                     { const int ln = fq * 16 + fr; ss += shx(ss, 16, ln); ss += shx(ss, 32, ln); }
;                     const float rstd = rsqrtf(ss * (1.f / 64.f) + EPS);
;                     const bool lat = row < NL; const int tok = row & 2047;
; #pragma unroll
;                     for (int bj = 0; bj < 2; ++bj) {
;                         f32x4 x1 = xf[bj][0] * rstd * w[bj][0], x2 = xf[bj][1] * rstd * w[bj][1];
;                         if (lat) { const int pos = bj ? (tok & 63) : (tok >> 6); const f32x4 c = *(const f32x4*)(ropec + pos * 16 + 4 * fq), s = *(const f32x4*)(ropes + pos * 16 + 4 * fq);
;                             const f32x4 o1 = x1 * c - x2 * s, o2 = x1 * s + x2 * c; x1 = o1; x2 = o2; }
;                         x1 = x1 * osc; x2 = x2 * osc;
;                         bf16_t* p = base + (size_t)row * 512 + 64 * hg + 32 * bj + 4 * fq;
;                         *(u32x2*)p = (u32x2){pk2(x1[0], x1[1]), pk2(x1[2], x1[3])};
;                         *(u32x2*)(p + 16) = (u32x2){pk2(x2[0], x2[1]), pk2(x2[2], x2[3])};
;                     }
.LBB0_316:
	s_or_b64 exec, exec, s[2:3]
	v_mov_b32_e32 v54, v118
	v_mov_b32_e32 v55, v118
	v_pk_mul_f32 v[38:39], v[54:55], v[38:39]
	v_pk_mul_f32 v[36:37], v[118:119], v[36:37]
	v_pk_mul_f32 v[56:57], v[54:55], v[56:57]
	v_pk_mul_f32 v[58:59], v[118:119], v[58:59]
	v_cvt_pk_bf16_f32 v36, v36, v37
	v_cvt_pk_bf16_f32 v37, v38, v39
	global_store_dwordx2 v[62:63], v[36:37], off offset:64
	v_cvt_pk_bf16_f32 v36, v58, v59
	v_cvt_pk_bf16_f32 v37, v56, v57
	global_store_dwordx2 v[62:63], v[36:37], off offset:96
	v_or_b32_e32 v36, 48, v102
	v_ashrrev_i32_e32 v37, 31, v36
	v_lshl_add_u64 v[38:39], v[36:37], 2, s[44:45]
	v_mov_b32_e32 v56, v223
	v_cvt_f32_i32_e32 v0, v2
	s_mov_b32 s2, 0x8000
	v_pk_mul_f32 v[16:17], v[16:17], v[56:57] op_sel_hi:[1,0]
	s_nop 0
	v_pk_mul_f32 v[38:39], v[16:17], v[50:51]
	v_pk_mul_f32 v[16:17], v[18:19], v[56:57] op_sel_hi:[1,0]
	v_pk_mul_f32 v[12:13], v[12:13], v[56:57] op_sel_hi:[1,0]
	v_pk_mul_f32 v[18:19], v[16:17], v[52:53]
	v_pk_mul_f32 v[16:17], v[12:13], v[46:47]
	v_pk_mul_f32 v[12:13], v[14:15], v[56:57] op_sel_hi:[1,0]
	v_mov_b32_e32 v46, v39
	v_mov_b32_e32 v47, v17
	v_pk_mul_f32 v[14:15], v[12:13], v[48:49]
	v_mov_b32_e32 v12, v38
	v_mov_b32_e32 v13, v16
	v_pk_mul_f32 v[46:47], v[46:47], v[46:47]
	v_pk_mul_f32 v[8:9], v[8:9], v[56:57] op_sel_hi:[1,0]
	v_pk_fma_f32 v[12:13], v[12:13], v[12:13], v[46:47]
	v_mov_b32_e32 v46, v18
	v_mov_b32_e32 v47, v14
	v_pk_fma_f32 v[12:13], v[46:47], v[46:47], v[12:13]
	v_mov_b32_e32 v46, v19
	v_mov_b32_e32 v47, v15
	v_pk_mul_f32 v[4:5], v[4:5], v[56:57] op_sel_hi:[1,0]
	v_pk_fma_f32 v[46:47], v[46:47], v[46:47], v[12:13]
	v_pk_mul_f32 v[12:13], v[8:9], v[42:43]
	v_pk_mul_f32 v[4:5], v[4:5], v[40:41]
	v_pk_mul_f32 v[2:3], v[6:7], v[56:57] op_sel_hi:[1,0]
	v_pk_mul_f32 v[8:9], v[10:11], v[56:57] op_sel_hi:[1,0]
	v_pk_mul_f32 v[6:7], v[2:3], v[0:1]
	v_mov_b32_e32 v2, v5
	v_mov_b32_e32 v3, v13
	v_pk_mul_f32 v[8:9], v[8:9], v[44:45]
	v_mov_b32_e32 v0, v4
	v_mov_b32_e32 v1, v12
	v_pk_mul_f32 v[2:3], v[2:3], v[2:3]
	s_nop 0
	v_pk_fma_f32 v[0:1], v[0:1], v[0:1], v[2:3]
	v_mov_b32_e32 v2, v6
	v_mov_b32_e32 v3, v8
	v_pk_fma_f32 v[0:1], v[2:3], v[2:3], v[0:1]
	v_mov_b32_e32 v2, v7
	v_mov_b32_e32 v3, v9
	v_pk_fma_f32 v[0:1], v[2:3], v[2:3], v[0:1]
	v_add_f32_e32 v2, v46, v47
	v_add_f32_e32 v1, v1, v2
	v_add_f32_e32 v0, v0, v1
	v_mov_b32_e32 v1, v0
	s_nop 1
	v_permlane16_swap_b32 v1, v0
	s_nop 0
	v_add_f32_e32 v0, v0, v1
	v_mov_b32_e32 v1, v0
	s_nop 1
	v_permlane32_swap_b32 v1, v0
	s_nop 0
	v_add_f32_e32 v0, v0, v1
	v_fmamk_f32 v0, v0, 0x3c800000, v246
	v_cmp_gt_f32_e32 vcc, s22, v0
	v_mul_f32_e32 v1, 0x4b800000, v0
	s_nop 0
	v_cndmask_b32_e32 v0, v0, v1, vcc
	v_rsq_f32_e32 v0, v0
	s_nop 0
	v_mul_f32_e32 v1, 0x45800000, v0
	v_cndmask_b32_e32 v10, v0, v1, vcc
	v_pk_mul_f32 v[0:1], v[38:39], v[10:11] op_sel_hi:[1,0]
	v_pk_mul_f32 v[2:3], v[18:19], v[10:11] op_sel_hi:[1,0]
	v_pk_mul_f32 v[18:19], v[16:17], v[10:11] op_sel_hi:[1,0]
	v_pk_mul_f32 v[14:15], v[14:15], v[10:11] op_sel_hi:[1,0]
	v_cmp_gt_i32_e32 vcc, s2, v36
	v_pk_mul_f32 v[2:3], v[34:35], v[2:3]
	v_pk_mul_f32 v[0:1], v[32:33], v[0:1]
	v_pk_mul_f32 v[16:17], v[30:31], v[14:15]
	v_pk_mul_f32 v[18:19], v[28:29], v[18:19]
	s_and_saveexec_b64 s[2:3], vcc
	s_cbranch_execz .LBB0_318
	s_and_b32 s30, s4, 0x7c0
	v_add_u32_e32 v14, s30, v225
	ds_read_b128 v[28:31], v14
	v_add_u32_e32 v14, s30, v225
	ds_read_b128 v[32:35], v14 offset:4096
	s_waitcnt lgkmcnt(1)
	v_pk_mul_f32 v[14:15], v[16:17], v[30:31]
	v_pk_mul_f32 v[38:39], v[18:19], v[28:29]
	v_pk_mul_f32 v[30:31], v[2:3], v[30:31]
	v_pk_mul_f32 v[28:29], v[0:1], v[28:29]
	s_waitcnt lgkmcnt(0)
	v_pk_fma_f32 v[2:3], v[2:3], v[34:35], v[14:15] neg_lo:[0,0,1] neg_hi:[0,0,1]
	v_pk_fma_f32 v[0:1], v[0:1], v[32:33], v[38:39] neg_lo:[0,0,1] neg_hi:[0,0,1]
	v_pk_fma_f32 v[16:17], v[16:17], v[34:35], v[30:31]
	v_pk_fma_f32 v[18:19], v[18:19], v[32:33], v[28:29]
